# phase 4: the scan-carry chains run on the 8 workgroups that have only one GEMM unit in this phase (were on workgroups 0-15 after their two units)
# baseline (speedup 1.0000x reference)
; DI void lru_carry(const Params& p, int G, int bid) {
;     const f32x2* SUMM = (const f32x2*)(p.ws + WS_SUMM); float* CARRY = (float*)(p.ws + WS_CARRY);
;     for (int gid = bid * NTHREADS + threadIdx.x; gid < 2 * NB * 1024; gid += G * NTHREADS) {
;         const int d = gid >> 12, b = (gid >> 10) & 3, ch = gid & 1023;
;         const size_t base = ((size_t)(d * NB + b) * NCHUNK) * 1024 + ch;
;         f32x2 sm[NCHUNK];
; #pragma unroll
;         for (int pos = 0; pos < NCHUNK; ++pos) { const int ci = d == 0 ? pos : (pos < 4 ? 3 - pos : 39 - pos); sm[pos] = SUMM[base + (size_t)ci * 1024]; }
;         float hh = 0.f;
; #pragma unroll
;         for (int pos = 0; pos < NCHUNK; ++pos) {
;             const int ci = d == 0 ? pos : (pos < 4 ? 3 - pos : 39 - pos);
;             CARRY[base + (size_t)ci * 1024] = hh;
;             hh = sm[pos][0] * hh + sm[pos][1];
;         }
;     }
; }
; __global__ void __launch_bounds__(NTHREADS, 2) fwd_kernel(Params p) {
;     ...
;         lru_carry(p, G, bid);
.LBB0_477:
	s_mov_b32 s1, s22
	s_cmpk_lg_i32 s23, 0x100
	s_cbranch_scc1 .Lcarry_hdr
	s_sub_i32 s1, s22, 0xf8
	s_cmp_lt_i32 s1, 0
	s_cselect_b32 s1, 0x7fff, s1
.Lcarry_hdr:
	v_lshl_or_b32 v1, s1, 9, v0
	s_movk_i32 s0, 0x2000
	v_cmp_gt_i32_e32 vcc, s0, v1
	s_and_saveexec_b64 s[2:3], vcc
	s_cbranch_execz .LBB0_480
	s_add_u32 s4, s50, 0x328ae000
	s_addc_u32 s5, s51, 0
	s_add_u32 s6, s50, 0x32aee000
	s_addc_u32 s7, s51, 0
	s_lshl_b32 s10, s23, 9
	s_cmpk_lg_i32 s23, 0x100
	s_cbranch_scc1 .Lcarry_st
	s_movk_i32 s10, 0x1000
.Lcarry_st:
	s_mov_b64 s[8:9], 0
	s_mov_b32 s11, 0xfffffc
	s_movk_i32 s12, 0x3ff
	s_movk_i32 s13, 0x1000
	v_mov_b32_e32 v3, 0
	v_mov_b32_e32 v6, 0x4000
	v_mov_b32_e32 v7, 0x23000
	s_movk_i32 s14, 0x1fff
